# MoE stagger plus one static s_setprio 1 for the odd (weight-block-first) waves during the K loops
# speedup vs baseline: 1.0029x; 1.0029x over previous
.Lmoe_Bp_1015:
	s_setprio 1

.Lmoe_X_1015:
	s_setprio 0
	s_waitcnt vmcnt(0)
	s_mov_b64 s[36:37], 0

.Lmoe_X_1019:
	s_setprio 0
	s_waitcnt vmcnt(0)
